# plus non-temporal loads for dead-after-use streams: dC^T in the mLSTM scan, C^T chunk image in mlstm_c
# baseline (speedup 1.0000x reference)
.LBB0_552:
	s_or_b64 exec, exec, s[26:27]
	s_ashr_i32 s25, s24, 31
	v_lshl_or_b32 v2, s50, 13, v147
	s_lshl_b64 s[10:11], s[24:25], 22
	v_or_b32_e32 v2, s10, v2
	v_mov_b32_e32 v3, s11
	v_lshl_add_u64 v[26:27], s[14:15], 0, v[2:3]
	v_add_co_u32_e32 v6, vcc, s39, v26
	s_waitcnt lgkmcnt(0)
	s_nop 0
	v_addc_co_u32_e32 v7, vcc, 0, v27, vcc
	v_add_co_u32_e32 v10, vcc, s40, v26
	s_barrier
	s_nop 0
	v_addc_co_u32_e32 v11, vcc, 0, v27, vcc
	v_add_co_u32_e32 v14, vcc, s41, v26
	s_nop 1
	v_addc_co_u32_e32 v15, vcc, 0, v27, vcc
	v_add_co_u32_e32 v18, vcc, s42, v26
	global_load_dwordx4 v[2:5], v[26:27], off nt
	s_nop 0
	global_load_dwordx4 v[6:9], v[6:7], off nt
	v_addc_co_u32_e32 v19, vcc, 0, v27, vcc
	v_add_co_u32_e32 v22, vcc, s43, v26
	global_load_dwordx4 v[10:13], v[10:11], off nt
	s_nop 0
	global_load_dwordx4 v[14:17], v[14:15], off nt
	v_addc_co_u32_e32 v23, vcc, 0, v27, vcc
	v_add_co_u32_e32 v28, vcc, s44, v26
	global_load_dwordx4 v[18:21], v[18:19], off nt
	s_nop 0
	global_load_dwordx4 v[22:25], v[22:23], off nt
	v_addc_co_u32_e32 v29, vcc, 0, v27, vcc
	s_waitcnt vmcnt(7)
	v_add_co_u32_e32 v30, vcc, s45, v26
	s_and_b32 s51, s48, 7
	s_nop 0
	v_addc_co_u32_e32 v31, vcc, 0, v27, vcc
	global_load_dwordx4 v[26:29], v[28:29], off nt
	s_nop 0
	global_load_dwordx4 v[30:33], v[30:31], off nt
	s_add_u32 s10, s31, s10
	v_lshl_or_b32 v134, s51, 13, v147
	s_addc_u32 s11, s33, s11
	v_mov_b32_e32 v138, 0
	s_mov_b32 s52, 0
	v_lshl_add_u64 v[136:137], s[10:11], 0, v[134:135]
	s_mov_b32 s53, 0
	v_mov_b32_e32 v139, v138
	v_mov_b32_e32 v140, v138
	v_mov_b32_e32 v141, v138
	v_mov_b32_e32 v142, v138
	v_mov_b32_e32 v143, v138
	v_mov_b32_e32 v144, v138
	v_mov_b32_e32 v145, v138
	s_branch .LBB0_554

.LBB0_554:
	s_cmp_lt_u32 s53, 56
	s_waitcnt vmcnt(0)
	v_mov_b64_e32 v[124:125], v[32:33]
	s_cselect_b64 s[28:29], -1, 0
	s_cmp_gt_u32 s53, 55
	v_mov_b64_e32 v[92:93], v[32:33]
	v_mov_b64_e32 v[96:97], v[4:5]
	v_mov_b64_e32 v[94:95], v[2:3]
	s_cselect_b64 s[26:27], -1, 0
	s_and_b64 vcc, exec, s[28:29]
	v_mov_b64_e32 v[90:91], v[30:31]
	v_mov_b64_e32 v[88:89], v[28:29]
	v_mov_b64_e32 v[86:87], v[26:27]
	v_mov_b64_e32 v[84:85], v[24:25]
	v_mov_b64_e32 v[82:83], v[22:23]
	v_mov_b64_e32 v[80:81], v[20:21]
	v_mov_b64_e32 v[78:79], v[18:19]
	v_mov_b64_e32 v[76:77], v[16:17]
	v_mov_b64_e32 v[74:75], v[14:15]
	v_mov_b64_e32 v[72:73], v[12:13]
	v_mov_b64_e32 v[70:71], v[10:11]
	v_mov_b64_e32 v[68:69], v[8:9]
	v_mov_b64_e32 v[66:67], v[6:7]
	v_mov_b64_e32 v[64:65], v[4:5]
	v_mov_b64_e32 v[62:63], v[2:3]
	v_mov_b32_e32 v126, v2
	v_mov_b32_e32 v128, v4
	v_mov_b64_e32 v[122:123], v[30:31]
	v_mov_b64_e32 v[120:121], v[28:29]
	v_mov_b64_e32 v[118:119], v[26:27]
	v_mov_b64_e32 v[116:117], v[24:25]
	v_mov_b64_e32 v[114:115], v[22:23]
	v_mov_b64_e32 v[112:113], v[20:21]
	v_mov_b64_e32 v[110:111], v[18:19]
	v_mov_b64_e32 v[108:109], v[16:17]
	v_mov_b64_e32 v[106:107], v[14:15]
	v_mov_b64_e32 v[104:105], v[12:13]
	v_mov_b64_e32 v[102:103], v[10:11]
	v_mov_b64_e32 v[100:101], v[8:9]
	v_mov_b64_e32 v[98:99], v[6:7]
	s_cbranch_vccz .LBB0_556
	global_load_dwordx4 v[126:129], v[136:137], off nt
	v_mov_b64_e32 v[92:93], v[32:33]
	v_mov_b64_e32 v[90:91], v[30:31]
	v_mov_b64_e32 v[88:89], v[28:29]
	v_mov_b64_e32 v[86:87], v[26:27]
	v_mov_b64_e32 v[84:85], v[24:25]
	v_mov_b64_e32 v[82:83], v[22:23]
	v_mov_b64_e32 v[80:81], v[20:21]
	v_mov_b64_e32 v[78:79], v[18:19]
	v_mov_b64_e32 v[76:77], v[16:17]
	v_mov_b64_e32 v[74:75], v[14:15]
	v_mov_b64_e32 v[72:73], v[12:13]
	v_mov_b64_e32 v[70:71], v[10:11]
	v_mov_b64_e32 v[68:69], v[8:9]
	v_mov_b64_e32 v[66:67], v[6:7]
	v_mov_b64_e32 v[64:65], v[4:5]
	v_mov_b64_e32 v[62:63], v[2:3]
	s_waitcnt vmcnt(0)
	v_mov_b32_e32 v3, v127
	v_mov_b32_e32 v5, v129
.LBB0_556:
	v_add_co_u32_e32 v38, vcc, 0x5f80000, v136
	v_cvt_pk_bf16_f32 v34, v144, v145
	v_cvt_pk_bf16_f32 v35, v142, v143
	v_cvt_pk_bf16_f32 v36, v140, v141
	v_cvt_pk_bf16_f32 v37, v138, v139
	v_addc_co_u32_e32 v39, vcc, 0, v137, vcc
	global_store_dwordx4 v[38:39], v[34:37], off
	s_andn2_b64 vcc, exec, s[28:29]
	s_nop 0
	v_mov_b32_e32 v34, s52
	ds_read2st64_b32 v[98:99], v34 offset1:1
	v_cndmask_b32_e64 v34, 0, 1, s[28:29]
	v_cmp_ne_u32_e64 s[10:11], 1, v34
	v_mov_b64_e32 v[34:35], v[62:63]
	v_mov_b64_e32 v[36:37], v[64:65]
	v_mov_b64_e32 v[38:39], v[66:67]
	v_mov_b64_e32 v[40:41], v[68:69]
	v_mov_b64_e32 v[42:43], v[70:71]
	v_mov_b64_e32 v[44:45], v[72:73]
	v_mov_b64_e32 v[46:47], v[74:75]
	v_mov_b64_e32 v[48:49], v[76:77]
	v_mov_b64_e32 v[50:51], v[78:79]
	v_mov_b64_e32 v[52:53], v[80:81]
	v_mov_b64_e32 v[54:55], v[82:83]
	v_mov_b64_e32 v[56:57], v[84:85]
	v_mov_b64_e32 v[58:59], v[86:87]
	v_mov_b64_e32 v[60:61], v[88:89]
	v_mov_b64_e32 v[62:63], v[90:91]
	v_mov_b64_e32 v[64:65], v[92:93]
	s_cbranch_vccnz .LBB0_558
	v_add_co_u32_e32 v6, vcc, 0x10000, v136
	s_nop 1
	v_addc_co_u32_e32 v7, vcc, 0, v137, vcc
	global_load_dwordx4 v[6:9], v[6:7], off nt
	s_waitcnt vmcnt(0)
	v_mov_b64_e32 v[64:65], v[32:33]
	v_mov_b64_e32 v[62:63], v[30:31]
	v_mov_b64_e32 v[60:61], v[28:29]
	v_mov_b64_e32 v[58:59], v[26:27]
	v_mov_b64_e32 v[56:57], v[24:25]
	v_mov_b64_e32 v[54:55], v[22:23]
	v_mov_b64_e32 v[52:53], v[20:21]
	v_mov_b64_e32 v[50:51], v[18:19]
	v_mov_b64_e32 v[48:49], v[16:17]
	v_mov_b64_e32 v[46:47], v[14:15]
	v_mov_b64_e32 v[44:45], v[12:13]
	v_mov_b64_e32 v[42:43], v[10:11]
	v_mov_b64_e32 v[36:37], v[4:5]
	v_mov_b64_e32 v[34:35], v[2:3]
	v_mov_b64_e32 v[40:41], v[8:9]
	v_mov_b64_e32 v[38:39], v[6:7]
.LBB0_558:
	v_lshlrev_b32_e32 v70, 16, v94
	v_and_b32_e32 v71, 0xffff0000, v2
	s_waitcnt lgkmcnt(0)
	v_mov_b32_e32 v2, v99
	v_lshlrev_b32_e32 v72, 16, v95
	v_and_b32_e32 v73, 0xffff0000, v95
	v_lshlrev_b32_e32 v74, 16, v96
	v_and_b32_e32 v75, 0xffff0000, v4
	v_lshlrev_b32_e32 v76, 16, v97
	v_and_b32_e32 v77, 0xffff0000, v97
	v_pk_mul_f32 v[70:71], v[2:3], v[70:71] op_sel_hi:[0,1]
	v_pk_mul_f32 v[72:73], v[2:3], v[72:73] op_sel_hi:[0,1]
	v_pk_mul_f32 v[74:75], v[2:3], v[74:75] op_sel_hi:[0,1]
	v_pk_mul_f32 v[76:77], v[2:3], v[76:77] op_sel_hi:[0,1]
	v_pk_fma_f32 v[70:71], v[144:145], v[98:99], v[70:71] op_sel_hi:[1,0,1]
	v_pk_fma_f32 v[72:73], v[142:143], v[98:99], v[72:73] op_sel_hi:[1,0,1]
	v_pk_fma_f32 v[74:75], v[140:141], v[98:99], v[74:75] op_sel_hi:[1,0,1]
	v_pk_fma_f32 v[76:77], v[138:139], v[98:99], v[76:77] op_sel_hi:[1,0,1]
	v_add_co_u32_e32 v82, vcc, 0x5f90000, v136
	v_cvt_pk_bf16_f32 v78, v70, v71
	v_cvt_pk_bf16_f32 v79, v72, v73
	v_cvt_pk_bf16_f32 v80, v74, v75
	v_cvt_pk_bf16_f32 v81, v76, v77
	v_addc_co_u32_e32 v83, vcc, 0, v137, vcc
	v_mov_b32_e32 v2, s52
	global_store_dwordx4 v[82:83], v[78:81], off
	ds_read2_b32 v[78:79], v2 offset0:1 offset1:65
	s_and_b64 vcc, exec, s[10:11]
	v_mov_b32_e32 v130, v10
	v_mov_b32_e32 v131, v11
	v_mov_b32_e32 v132, v12
	v_mov_b32_e32 v133, v13
	s_cbranch_vccnz .LBB0_560
	v_add_co_u32_e32 v34, vcc, 0x20000, v136
	s_nop 1
	v_addc_co_u32_e32 v35, vcc, 0, v137, vcc
	global_load_dwordx4 v[130:133], v[34:35], off nt
	v_mov_b64_e32 v[64:65], v[32:33]
	v_mov_b64_e32 v[62:63], v[30:31]
	v_mov_b64_e32 v[60:61], v[28:29]
	v_mov_b64_e32 v[58:59], v[26:27]
	v_mov_b64_e32 v[56:57], v[24:25]
	v_mov_b64_e32 v[54:55], v[22:23]
	v_mov_b64_e32 v[52:53], v[20:21]
	v_mov_b64_e32 v[50:51], v[18:19]
	v_mov_b64_e32 v[48:49], v[16:17]
	v_mov_b64_e32 v[46:47], v[14:15]
	v_mov_b64_e32 v[44:45], v[12:13]
	v_mov_b64_e32 v[42:43], v[10:11]
	v_mov_b64_e32 v[40:41], v[8:9]
	v_mov_b64_e32 v[38:39], v[6:7]
	v_mov_b64_e32 v[36:37], v[4:5]
	v_mov_b64_e32 v[34:35], v[2:3]
.LBB0_560:
	v_lshlrev_b32_e32 v80, 16, v66
	v_and_b32_e32 v81, 0xffff0000, v66
	s_waitcnt lgkmcnt(0)
	v_mov_b32_e32 v2, v79
	v_lshlrev_b32_e32 v66, 16, v67
	v_and_b32_e32 v67, 0xffff0000, v67
	v_pk_mul_f32 v[66:67], v[2:3], v[66:67] op_sel_hi:[0,1]
	v_pk_fma_f32 v[84:85], v[72:73], v[78:79], v[66:67] op_sel_hi:[1,0,1]
	v_lshlrev_b32_e32 v66, 16, v68
	v_and_b32_e32 v67, 0xffff0000, v68
	v_pk_mul_f32 v[66:67], v[2:3], v[66:67] op_sel_hi:[0,1]
	v_pk_fma_f32 v[86:87], v[74:75], v[78:79], v[66:67] op_sel_hi:[1,0,1]
	v_lshlrev_b32_e32 v66, 16, v69
	v_and_b32_e32 v67, 0xffff0000, v69
	v_pk_mul_f32 v[80:81], v[2:3], v[80:81] op_sel_hi:[0,1]
	v_pk_mul_f32 v[66:67], v[2:3], v[66:67] op_sel_hi:[0,1]
	v_mov_b32_e32 v2, s52
	ds_read2_b32 v[90:91], v2 offset0:2 offset1:66
	v_pk_fma_f32 v[82:83], v[70:71], v[78:79], v[80:81] op_sel_hi:[1,0,1]
	v_pk_fma_f32 v[88:89], v[76:77], v[78:79], v[66:67] op_sel_hi:[1,0,1]
	v_add_co_u32_e32 v70, vcc, 0x5fa0000, v136
	v_cvt_pk_bf16_f32 v66, v82, v83
	v_cvt_pk_bf16_f32 v67, v84, v85
	v_cvt_pk_bf16_f32 v68, v86, v87
	v_cvt_pk_bf16_f32 v69, v88, v89
	v_addc_co_u32_e32 v71, vcc, 0, v137, vcc
	global_store_dwordx4 v[70:71], v[66:69], off
	v_mov_b64_e32 v[80:81], v[64:65]
	s_and_b64 vcc, exec, s[10:11]
	v_mov_b64_e32 v[78:79], v[62:63]
	v_mov_b64_e32 v[76:77], v[60:61]
	v_mov_b64_e32 v[74:75], v[58:59]
	v_mov_b64_e32 v[72:73], v[56:57]
	v_mov_b64_e32 v[70:71], v[54:55]
	v_mov_b64_e32 v[68:69], v[52:53]
	v_mov_b64_e32 v[66:67], v[50:51]
	v_mov_b64_e32 v[64:65], v[48:49]
	v_mov_b64_e32 v[62:63], v[46:47]
	v_mov_b64_e32 v[60:61], v[44:45]
	v_mov_b64_e32 v[58:59], v[42:43]
	v_mov_b64_e32 v[56:57], v[40:41]
	v_mov_b64_e32 v[54:55], v[38:39]
	v_mov_b64_e32 v[52:53], v[36:37]
	v_mov_b64_e32 v[50:51], v[34:35]
	s_cbranch_vccnz .LBB0_562
	v_add_co_u32_e32 v14, vcc, 0x30000, v136
	s_nop 1
	v_addc_co_u32_e32 v15, vcc, 0, v137, vcc
	global_load_dwordx4 v[14:17], v[14:15], off nt
	s_waitcnt vmcnt(0)
	v_mov_b64_e32 v[80:81], v[32:33]
	v_mov_b64_e32 v[78:79], v[30:31]
	v_mov_b64_e32 v[76:77], v[28:29]
	v_mov_b64_e32 v[74:75], v[26:27]
	v_mov_b64_e32 v[72:73], v[24:25]
	v_mov_b64_e32 v[70:71], v[22:23]
	v_mov_b64_e32 v[68:69], v[20:21]
	v_mov_b64_e32 v[66:67], v[18:19]
	v_mov_b64_e32 v[60:61], v[12:13]
	v_mov_b64_e32 v[58:59], v[10:11]
	v_mov_b64_e32 v[56:57], v[8:9]
	v_mov_b64_e32 v[54:55], v[6:7]
	v_mov_b64_e32 v[52:53], v[4:5]
	v_mov_b64_e32 v[50:51], v[2:3]
	v_mov_b64_e32 v[64:65], v[16:17]
	v_mov_b64_e32 v[62:63], v[14:15]
.LBB0_562:
	v_lshlrev_b32_e32 v34, 16, v10
	v_and_b32_e32 v35, 0xffff0000, v10
	s_waitcnt lgkmcnt(0)
	v_mov_b32_e32 v2, v91
	v_lshlrev_b32_e32 v10, 16, v11
	v_and_b32_e32 v11, 0xffff0000, v11
	v_lshlrev_b32_e32 v36, 16, v12
	v_and_b32_e32 v37, 0xffff0000, v12
	v_lshlrev_b32_e32 v12, 16, v13
	v_and_b32_e32 v13, 0xffff0000, v13
	v_pk_mul_f32 v[34:35], v[2:3], v[34:35] op_sel_hi:[0,1]
	v_pk_mul_f32 v[10:11], v[2:3], v[10:11] op_sel_hi:[0,1]
	v_pk_mul_f32 v[36:37], v[2:3], v[36:37] op_sel_hi:[0,1]
	v_pk_mul_f32 v[12:13], v[2:3], v[12:13] op_sel_hi:[0,1]
	v_mov_b32_e32 v2, s52
	ds_read2_b32 v[38:39], v2 offset0:3 offset1:67
	v_add_co_u32_e32 v44, vcc, 0x5fb0000, v136
	v_pk_fma_f32 v[34:35], v[82:83], v[90:91], v[34:35] op_sel_hi:[1,0,1]
	v_pk_fma_f32 v[10:11], v[84:85], v[90:91], v[10:11] op_sel_hi:[1,0,1]
	v_pk_fma_f32 v[36:37], v[86:87], v[90:91], v[36:37] op_sel_hi:[1,0,1]
	v_pk_fma_f32 v[12:13], v[88:89], v[90:91], v[12:13] op_sel_hi:[1,0,1]
	v_addc_co_u32_e32 v45, vcc, 0, v137, vcc
	v_mov_b64_e32 v[100:101], v[80:81]
	v_cvt_pk_bf16_f32 v40, v34, v35
	v_cvt_pk_bf16_f32 v41, v10, v11
	v_cvt_pk_bf16_f32 v42, v36, v37
	v_cvt_pk_bf16_f32 v43, v12, v13
	s_and_b64 vcc, exec, s[10:11]
	v_mov_b64_e32 v[98:99], v[78:79]
	v_mov_b64_e32 v[96:97], v[76:77]
	v_mov_b64_e32 v[94:95], v[74:75]
	v_mov_b64_e32 v[92:93], v[72:73]
	v_mov_b64_e32 v[90:91], v[70:71]
	v_mov_b64_e32 v[88:89], v[68:69]
	v_mov_b64_e32 v[86:87], v[66:67]
	v_mov_b64_e32 v[84:85], v[64:65]
	v_mov_b64_e32 v[82:83], v[62:63]
	v_mov_b64_e32 v[80:81], v[60:61]
	v_mov_b64_e32 v[78:79], v[58:59]
	v_mov_b64_e32 v[76:77], v[56:57]
	v_mov_b64_e32 v[74:75], v[54:55]
	v_mov_b64_e32 v[72:73], v[52:53]
	v_mov_b64_e32 v[70:71], v[50:51]
	global_store_dwordx4 v[44:45], v[40:43], off
	s_cbranch_vccnz .LBB0_564
	v_add_co_u32_e32 v18, vcc, 0x40000, v136
	s_nop 1
	v_addc_co_u32_e32 v19, vcc, 0, v137, vcc
	global_load_dwordx4 v[18:21], v[18:19], off nt
	s_waitcnt vmcnt(0)
	v_mov_b64_e32 v[100:101], v[32:33]
	v_mov_b64_e32 v[98:99], v[30:31]
	v_mov_b64_e32 v[96:97], v[28:29]
	v_mov_b64_e32 v[94:95], v[26:27]
	v_mov_b64_e32 v[92:93], v[24:25]
	v_mov_b64_e32 v[90:91], v[22:23]
	v_mov_b64_e32 v[84:85], v[16:17]
	v_mov_b64_e32 v[82:83], v[14:15]
	v_mov_b64_e32 v[80:81], v[12:13]
	v_mov_b64_e32 v[78:79], v[10:11]
	v_mov_b64_e32 v[76:77], v[8:9]
	v_mov_b64_e32 v[74:75], v[6:7]
	v_mov_b64_e32 v[72:73], v[4:5]
	v_mov_b64_e32 v[70:71], v[2:3]
	v_mov_b64_e32 v[88:89], v[20:21]
	v_mov_b64_e32 v[86:87], v[18:19]
.LBB0_564:
	s_nop 0
	v_lshlrev_b32_e32 v40, 16, v46
	v_and_b32_e32 v41, 0xffff0000, v46
	s_waitcnt lgkmcnt(0)
	v_mov_b32_e32 v2, v39
	v_pk_mul_f32 v[40:41], v[2:3], v[40:41] op_sel_hi:[0,1]
	v_pk_fma_f32 v[102:103], v[34:35], v[38:39], v[40:41] op_sel_hi:[1,0,1]
	v_lshlrev_b32_e32 v34, 16, v47
	v_and_b32_e32 v35, 0xffff0000, v47
	v_pk_mul_f32 v[34:35], v[2:3], v[34:35] op_sel_hi:[0,1]
	v_pk_fma_f32 v[10:11], v[10:11], v[38:39], v[34:35] op_sel_hi:[1,0,1]
	v_lshlrev_b32_e32 v34, 16, v48
	v_and_b32_e32 v35, 0xffff0000, v48
	v_pk_mul_f32 v[34:35], v[2:3], v[34:35] op_sel_hi:[0,1]
	v_pk_fma_f32 v[104:105], v[36:37], v[38:39], v[34:35] op_sel_hi:[1,0,1]
	v_lshlrev_b32_e32 v34, 16, v49
	v_and_b32_e32 v35, 0xffff0000, v49
	v_pk_mul_f32 v[34:35], v[2:3], v[34:35] op_sel_hi:[0,1]
	v_mov_b32_e32 v2, s52
	ds_read2_b32 v[106:107], v2 offset0:4 offset1:68
	v_pk_fma_f32 v[12:13], v[12:13], v[38:39], v[34:35] op_sel_hi:[1,0,1]
	v_add_co_u32_e32 v38, vcc, 0x5fc0000, v136
	v_cvt_pk_bf16_f32 v34, v102, v103
	v_cvt_pk_bf16_f32 v35, v10, v11
	v_cvt_pk_bf16_f32 v36, v104, v105
	v_cvt_pk_bf16_f32 v37, v12, v13
	v_addc_co_u32_e32 v39, vcc, 0, v137, vcc
	global_store_dwordx4 v[38:39], v[34:37], off
	s_and_b64 vcc, exec, s[10:11]
	s_nop 0
	v_mov_b64_e32 v[34:35], v[70:71]
	v_mov_b64_e32 v[36:37], v[72:73]
	v_mov_b64_e32 v[38:39], v[74:75]
	v_mov_b64_e32 v[40:41], v[76:77]
	v_mov_b64_e32 v[42:43], v[78:79]
	v_mov_b64_e32 v[44:45], v[80:81]
	v_mov_b64_e32 v[46:47], v[82:83]
	v_mov_b64_e32 v[48:49], v[84:85]
	v_mov_b64_e32 v[50:51], v[86:87]
	v_mov_b64_e32 v[52:53], v[88:89]
	v_mov_b64_e32 v[54:55], v[90:91]
	v_mov_b64_e32 v[56:57], v[92:93]
	v_mov_b64_e32 v[58:59], v[94:95]
	v_mov_b64_e32 v[60:61], v[96:97]
	v_mov_b64_e32 v[62:63], v[98:99]
	v_mov_b64_e32 v[64:65], v[100:101]
	s_cbranch_vccnz .LBB0_566
	v_add_co_u32_e32 v22, vcc, 0x50000, v136
	s_nop 1
	v_addc_co_u32_e32 v23, vcc, 0, v137, vcc
	global_load_dwordx4 v[22:25], v[22:23], off nt
	s_waitcnt vmcnt(0)
	v_mov_b64_e32 v[64:65], v[32:33]
	v_mov_b64_e32 v[62:63], v[30:31]
	v_mov_b64_e32 v[60:61], v[28:29]
	v_mov_b64_e32 v[58:59], v[26:27]
	v_mov_b64_e32 v[52:53], v[20:21]
	v_mov_b64_e32 v[50:51], v[18:19]
	v_mov_b64_e32 v[48:49], v[16:17]
	v_mov_b64_e32 v[46:47], v[14:15]
	v_mov_b64_e32 v[44:45], v[12:13]
	v_mov_b64_e32 v[42:43], v[10:11]
	v_mov_b64_e32 v[40:41], v[8:9]
	v_mov_b64_e32 v[38:39], v[6:7]
	v_mov_b64_e32 v[36:37], v[4:5]
	v_mov_b64_e32 v[34:35], v[2:3]
	v_mov_b64_e32 v[56:57], v[24:25]
	v_mov_b64_e32 v[54:55], v[22:23]
.LBB0_566:
	v_lshlrev_b32_e32 v70, 16, v66
	v_and_b32_e32 v71, 0xffff0000, v66
	s_waitcnt lgkmcnt(0)
	v_mov_b32_e32 v2, v107
	v_lshlrev_b32_e32 v66, 16, v67
	v_and_b32_e32 v67, 0xffff0000, v67
	v_pk_mul_f32 v[66:67], v[2:3], v[66:67] op_sel_hi:[0,1]
	v_pk_fma_f32 v[10:11], v[10:11], v[106:107], v[66:67] op_sel_hi:[1,0,1]
	v_lshlrev_b32_e32 v66, 16, v68
	v_and_b32_e32 v67, 0xffff0000, v68
	v_lshlrev_b32_e32 v68, 16, v69
	v_and_b32_e32 v69, 0xffff0000, v69
	v_pk_mul_f32 v[70:71], v[2:3], v[70:71] op_sel_hi:[0,1]
	v_pk_mul_f32 v[66:67], v[2:3], v[66:67] op_sel_hi:[0,1]
	v_pk_mul_f32 v[68:69], v[2:3], v[68:69] op_sel_hi:[0,1]
	v_mov_b32_e32 v2, s52
	v_pk_fma_f32 v[12:13], v[12:13], v[106:107], v[68:69] op_sel_hi:[1,0,1]
	ds_read2_b32 v[68:69], v2 offset0:5 offset1:69
	v_add_co_u32_e32 v76, vcc, 0x5fd0000, v136
	v_pk_fma_f32 v[70:71], v[102:103], v[106:107], v[70:71] op_sel_hi:[1,0,1]
	v_pk_fma_f32 v[66:67], v[104:105], v[106:107], v[66:67] op_sel_hi:[1,0,1]
	v_addc_co_u32_e32 v77, vcc, 0, v137, vcc
	v_mov_b64_e32 v[124:125], v[64:65]
	v_cvt_pk_bf16_f32 v72, v70, v71
	v_cvt_pk_bf16_f32 v73, v10, v11
	v_cvt_pk_bf16_f32 v74, v66, v67
	v_cvt_pk_bf16_f32 v75, v12, v13
	s_and_b64 vcc, exec, s[10:11]
	v_mov_b64_e32 v[122:123], v[62:63]
	global_store_dwordx4 v[76:77], v[72:75], off
	v_mov_b64_e32 v[120:121], v[60:61]
	v_mov_b64_e32 v[118:119], v[58:59]
	v_mov_b64_e32 v[116:117], v[56:57]
	v_mov_b64_e32 v[114:115], v[54:55]
	v_mov_b64_e32 v[112:113], v[52:53]
	v_mov_b64_e32 v[110:111], v[50:51]
	v_mov_b64_e32 v[108:109], v[48:49]
	v_mov_b64_e32 v[106:107], v[46:47]
	v_mov_b64_e32 v[104:105], v[44:45]
	v_mov_b64_e32 v[102:103], v[42:43]
	v_mov_b64_e32 v[100:101], v[40:41]
	v_mov_b64_e32 v[98:99], v[38:39]
	v_mov_b64_e32 v[96:97], v[36:37]
	v_mov_b64_e32 v[94:95], v[34:35]
	s_cbranch_vccnz .LBB0_568
	v_add_co_u32_e32 v26, vcc, 0x60000, v136
	s_nop 1
	v_addc_co_u32_e32 v27, vcc, 0, v137, vcc
	global_load_dwordx4 v[26:29], v[26:27], off nt
	s_waitcnt vmcnt(0)
	v_mov_b64_e32 v[124:125], v[32:33]
	v_mov_b64_e32 v[122:123], v[30:31]
	v_mov_b64_e32 v[116:117], v[24:25]
	v_mov_b64_e32 v[114:115], v[22:23]
	v_mov_b64_e32 v[112:113], v[20:21]
	v_mov_b64_e32 v[110:111], v[18:19]
	v_mov_b64_e32 v[108:109], v[16:17]
	v_mov_b64_e32 v[106:107], v[14:15]
	v_mov_b64_e32 v[104:105], v[12:13]
	v_mov_b64_e32 v[102:103], v[10:11]
	v_mov_b64_e32 v[100:101], v[8:9]
	v_mov_b64_e32 v[98:99], v[6:7]
	v_mov_b64_e32 v[96:97], v[4:5]
	v_mov_b64_e32 v[94:95], v[2:3]
	v_mov_b64_e32 v[120:121], v[28:29]
	v_mov_b64_e32 v[118:119], v[26:27]
.LBB0_568:
	s_waitcnt lgkmcnt(0)
	v_mov_b32_e32 v2, v69
	v_lshlrev_b32_e32 v36, 16, v91
	v_and_b32_e32 v37, 0xffff0000, v91
	v_pk_mul_f32 v[36:37], v[2:3], v[36:37] op_sel_hi:[0,1]
	v_lshlrev_b32_e32 v34, 16, v90
	v_and_b32_e32 v35, 0xffff0000, v90
	v_pk_fma_f32 v[10:11], v[10:11], v[68:69], v[36:37] op_sel_hi:[1,0,1]
	v_lshlrev_b32_e32 v36, 16, v92
	v_and_b32_e32 v37, 0xffff0000, v92
	v_lshlrev_b32_e32 v38, 16, v93
	v_and_b32_e32 v39, 0xffff0000, v93
	v_pk_mul_f32 v[34:35], v[2:3], v[34:35] op_sel_hi:[0,1]
	v_pk_mul_f32 v[36:37], v[2:3], v[36:37] op_sel_hi:[0,1]
	v_pk_mul_f32 v[38:39], v[2:3], v[38:39] op_sel_hi:[0,1]
	v_mov_b32_e32 v2, s52
	v_pk_fma_f32 v[12:13], v[12:13], v[68:69], v[38:39] op_sel_hi:[1,0,1]
	ds_read2_b32 v[38:39], v2 offset0:6 offset1:70
	v_add_co_u32_e32 v44, vcc, 0x5fe0000, v136
	v_pk_fma_f32 v[34:35], v[70:71], v[68:69], v[34:35] op_sel_hi:[1,0,1]
	v_pk_fma_f32 v[36:37], v[66:67], v[68:69], v[36:37] op_sel_hi:[1,0,1]
	v_addc_co_u32_e32 v45, vcc, 0, v137, vcc
	v_cvt_pk_bf16_f32 v40, v34, v35
	v_cvt_pk_bf16_f32 v41, v10, v11
	v_cvt_pk_bf16_f32 v42, v36, v37
	v_cvt_pk_bf16_f32 v43, v12, v13
	s_and_b64 vcc, exec, s[10:11]
	global_store_dwordx4 v[44:45], v[40:43], off
	s_cbranch_vccnz .LBB0_553
	v_add_co_u32_e32 v30, vcc, 0x70000, v136
	s_nop 1
	v_addc_co_u32_e32 v31, vcc, 0, v137, vcc
	global_load_dwordx4 v[30:33], v[30:31], off nt
	s_branch .LBB0_553

.LBB0_659:
	s_ashr_i32 s70, s39, 6
	s_ashr_i32 s71, s70, 31
	s_and_b32 s74, s33, 0x1f80
	s_lshl_b64 s[30:31], s[70:71], 22
	v_lshl_add_u64 v[50:51], v[162:163], 0, s[30:31]
	s_lshl_b32 s88, s74, 1
	v_lshl_add_u64 v[50:51], v[50:51], 0, s[88:89]
	v_lshl_add_u64 v[94:95], v[50:51], 0, v[160:161]
	global_load_dword v114, v[198:199], off
	global_load_dwordx4 v[50:53], v[94:95], off offset:48
	global_load_dwordx4 v[54:57], v[94:95], off offset:32
	global_load_dwordx4 v[58:61], v[94:95], off offset:16
	global_load_dwordx4 v[62:65], v[94:95], off
	global_load_dwordx4 v[66:69], v[200:201], off offset:-16 nt
	global_load_dwordx4 v[70:73], v[200:201], off offset:-32 nt
	global_load_dwordx4 v[74:77], v[200:201], off offset:-48 nt
	global_load_dwordx4 v[78:81], v[200:201], off offset:-64 nt
	global_load_dwordx4 v[82:85], v[94:95], off offset:112
	global_load_dwordx4 v[86:89], v[94:95], off offset:96
	global_load_dwordx4 v[90:93], v[94:95], off offset:80
	s_nop 0
	global_load_dwordx4 v[94:97], v[94:95], off offset:64
	s_nop 0
	global_load_dwordx4 v[98:101], v[200:201], off offset:48 nt
	global_load_dwordx4 v[102:105], v[200:201], off offset:32 nt
	global_load_dwordx4 v[106:109], v[200:201], off offset:16 nt
	global_load_dwordx4 v[110:113], v[200:201], off nt
	s_mul_hi_i32 s30, s70, 0x2aaaaaab
	s_lshr_b32 s31, s30, 31
	s_add_i32 s72, s30, s31
	s_ashr_i32 s73, s72, 31
	s_lshl_b64 s[30:31], s[72:73], 13
	s_or_b32 s30, s30, s74
	s_mul_i32 s71, s72, 6
	v_lshl_add_u64 v[204:205], s[30:31], 0, v[164:165]
	v_mov_b64_e32 v[252:253], s[92:93]
	s_sub_i32 s88, s70, s71
	v_mad_u64_u32 v[252:253], s[70:71], v204, s3, v[252:253]
	s_lshl_b32 s70, s88, 7
	s_ashr_i32 s71, s70, 31
	v_mad_i32_i24 v253, v205, s3, v253
	s_lshl_b64 s[70:71], s[70:71], 1
	v_lshl_add_u64 v[252:253], v[252:253], 0, s[70:71]
	v_mov_b32_e32 v203, v161
	v_lshl_add_u64 v[244:245], v[252:253], 0, v[202:203]
	global_load_dwordx4 v[232:235], v[244:245], off
	global_load_dwordx4 v[236:239], v[244:245], off offset:64
	global_load_dwordx4 v[240:243], v[244:245], off offset:128
	global_load_dwordx4 v[248:251], v[244:245], off offset:192
	global_load_dword v210, v161, s[22:23]
	s_waitcnt vmcnt(21)
	ds_write_b32 v1, v114
	s_waitcnt vmcnt(17)
	ds_write_b128 v183, v[62:65]
	s_waitcnt vmcnt(13)
	ds_write_b128 v212, v[78:81]
	ds_write_b128 v183, v[58:61] offset:16
	ds_write_b128 v212, v[74:77] offset:16
	ds_write_b128 v183, v[54:57] offset:32
	ds_write_b128 v212, v[70:73] offset:32
	ds_write_b128 v183, v[50:53] offset:48
	ds_write_b128 v212, v[66:69] offset:48
	s_waitcnt vmcnt(9)
	ds_write_b128 v183, v[94:97] offset:64
	s_waitcnt vmcnt(5)
	ds_write_b128 v212, v[110:113] offset:64
	ds_write_b128 v183, v[90:93] offset:80
	ds_write_b128 v212, v[106:109] offset:80
	ds_write_b128 v183, v[86:89] offset:96
	ds_write_b128 v212, v[102:105] offset:96
	ds_write_b128 v183, v[82:85] offset:112
	ds_write_b128 v212, v[98:101] offset:112
	s_waitcnt lgkmcnt(0)
	s_barrier
	ds_read_b32 v130, v159
	ds_read_b32 v208, v171
	ds_read_b128 v[54:57], v173
	ds_read_b128 v[58:61], v173 offset:16
	v_lshl_add_u64 v[138:139], v[166:167], 0, s[70:71]
	v_or_b32_e32 v131, s30, v158
	s_andn2_b64 vcc, exec, s[94:95]
	ds_read_b128 v[74:77], v213 offset:4416
	ds_read_b128 v[78:81], v213 offset:8768
	ds_read_b128 v[82:85], v213 offset:13120
	s_waitcnt vmcnt(0)
	v_mov_b32_e32 v50, v232
	v_mov_b32_e32 v51, v233
	v_mov_b32_e32 v52, v234
	v_mov_b32_e32 v53, v235
	v_and_b32_e32 v65, 0xffff0000, v50
	v_lshlrev_b32_e32 v64, 16, v50
	s_waitcnt lgkmcnt(4)
	v_mul_f32_e32 v55, v55, v65
	v_fmac_f32_e32 v55, v54, v64
	v_lshlrev_b32_e32 v54, 16, v51
	v_fmac_f32_e32 v55, v56, v54
	v_and_b32_e32 v54, 0xffff0000, v51
	v_fmac_f32_e32 v55, v57, v54
	v_lshlrev_b32_e32 v54, 16, v52
	s_waitcnt lgkmcnt(3)
	v_fmac_f32_e32 v55, v58, v54
	v_and_b32_e32 v54, 0xffff0000, v52
	v_fmac_f32_e32 v55, v59, v54
	v_lshlrev_b32_e32 v54, 16, v53
	v_fmac_f32_e32 v55, v60, v54
	v_and_b32_e32 v54, 0xffff0000, v53
	v_fmac_f32_e32 v55, v61, v54
	v_add_f32_e32 v64, 0, v55
	ds_read_b128 v[58:61], v173 offset:128
	v_mov_b32_e32 v54, v236
	v_mov_b32_e32 v55, v237
	v_mov_b32_e32 v56, v238
	v_mov_b32_e32 v57, v239
	v_and_b32_e32 v66, 0xffff0000, v54
	v_lshlrev_b32_e32 v65, 16, v54
	s_waitcnt lgkmcnt(0)
	v_mul_f32_e32 v66, v59, v66
	v_fmac_f32_e32 v66, v58, v65
	v_lshlrev_b32_e32 v58, 16, v55
	v_fmac_f32_e32 v66, v60, v58
	v_and_b32_e32 v58, 0xffff0000, v55
	v_fmac_f32_e32 v66, v61, v58
	ds_read_b128 v[58:61], v173 offset:144
	v_lshlrev_b32_e32 v65, 16, v56
	s_waitcnt lgkmcnt(0)
	v_fmac_f32_e32 v66, v58, v65
	v_and_b32_e32 v58, 0xffff0000, v56
	v_fmac_f32_e32 v66, v59, v58
	v_lshlrev_b32_e32 v58, 16, v57
	v_fmac_f32_e32 v66, v60, v58
	v_and_b32_e32 v58, 0xffff0000, v57
	v_fmac_f32_e32 v66, v61, v58
	v_add_f32_e32 v68, v64, v66
	ds_read_b128 v[64:67], v173 offset:256
	v_mov_b32_e32 v58, v240
	v_mov_b32_e32 v59, v241
	v_mov_b32_e32 v60, v242
	v_mov_b32_e32 v61, v243
	v_and_b32_e32 v70, 0xffff0000, v58
	v_lshlrev_b32_e32 v69, 16, v58
	s_waitcnt lgkmcnt(0)
	v_mul_f32_e32 v70, v65, v70
	v_fmac_f32_e32 v70, v64, v69
	v_lshlrev_b32_e32 v64, 16, v59
	v_fmac_f32_e32 v70, v66, v64
	v_and_b32_e32 v64, 0xffff0000, v59
	v_fmac_f32_e32 v70, v67, v64
	ds_read_b128 v[64:67], v173 offset:272
	v_lshlrev_b32_e32 v69, 16, v60
	s_waitcnt lgkmcnt(0)
	v_fmac_f32_e32 v70, v64, v69
	v_and_b32_e32 v64, 0xffff0000, v60
	v_fmac_f32_e32 v70, v65, v64
	v_lshlrev_b32_e32 v64, 16, v61
	v_fmac_f32_e32 v70, v66, v64
	v_and_b32_e32 v64, 0xffff0000, v61
	v_fmac_f32_e32 v70, v67, v64
	v_add_f32_e32 v66, v68, v70
	ds_read_b128 v[62:65], v173 offset:384
	v_mov_b32_e32 v70, v248
	v_mov_b32_e32 v71, v249
	v_mov_b32_e32 v72, v250
	v_mov_b32_e32 v73, v251
	v_and_b32_e32 v68, 0xffff0000, v70
	v_lshlrev_b32_e32 v67, 16, v70
	s_waitcnt lgkmcnt(0)
	v_mul_f32_e32 v68, v63, v68
	v_fmac_f32_e32 v68, v62, v67
	v_lshlrev_b32_e32 v62, 16, v71
	v_fmac_f32_e32 v68, v64, v62
	v_and_b32_e32 v62, 0xffff0000, v71
	v_fmac_f32_e32 v68, v65, v62
	ds_read_b128 v[62:65], v173 offset:400
	v_lshlrev_b32_e32 v67, 16, v72
	s_waitcnt lgkmcnt(0)
	v_fmac_f32_e32 v68, v62, v67
	v_and_b32_e32 v62, 0xffff0000, v72
	v_fmac_f32_e32 v68, v63, v62
	v_lshlrev_b32_e32 v62, 16, v73
	v_fmac_f32_e32 v68, v64, v62
	v_and_b32_e32 v62, 0xffff0000, v73
	v_fmac_f32_e32 v68, v65, v62
	v_add_f32_e32 v62, v66, v68
	ds_bpermute_b32 v63, v175, v62
	ds_read_b128 v[66:69], v213 offset:64
	s_waitcnt lgkmcnt(1)
	v_add_f32_e32 v203, v62, v63
	ds_read_b128 v[62:65], v213
	s_waitcnt lgkmcnt(0)
	v_mfma_f32_16x16x32_bf16 v[62:65], v[62:65], v[50:53], 0
	ds_bpermute_b32 v209, v177, v203
	v_mfma_f32_16x16x32_bf16 v[62:65], v[66:69], v[54:57], v[62:65]
	ds_read_b128 v[66:69], v213 offset:128
	s_waitcnt lgkmcnt(0)
	v_mfma_f32_16x16x32_bf16 v[62:65], v[66:69], v[58:61], v[62:65]
	ds_read_b128 v[66:69], v213 offset:192
	s_waitcnt lgkmcnt(0)
	v_mfma_f32_16x16x32_bf16 v[62:65], v[66:69], v[70:73], v[62:65]
	ds_read_b128 v[66:69], v213 offset:4352
	s_waitcnt lgkmcnt(0)
	v_mfma_f32_16x16x32_bf16 v[66:69], v[66:69], v[50:53], 0
	v_mfma_f32_16x16x32_bf16 v[66:69], v[74:77], v[54:57], v[66:69]
	ds_read_b128 v[74:77], v213 offset:4480
	s_waitcnt lgkmcnt(0)
	v_mfma_f32_16x16x32_bf16 v[66:69], v[74:77], v[58:61], v[66:69]
	ds_read_b128 v[74:77], v213 offset:4544
	s_waitcnt lgkmcnt(0)
	v_mfma_f32_16x16x32_bf16 v[66:69], v[74:77], v[70:73], v[66:69]
	ds_read_b128 v[74:77], v213 offset:8704
	s_waitcnt lgkmcnt(0)
	v_mfma_f32_16x16x32_bf16 v[74:77], v[74:77], v[50:53], 0
	v_mfma_f32_16x16x32_bf16 v[74:77], v[78:81], v[54:57], v[74:77]
	ds_read_b128 v[78:81], v213 offset:8832
	s_waitcnt lgkmcnt(0)
	v_mfma_f32_16x16x32_bf16 v[74:77], v[78:81], v[58:61], v[74:77]
	ds_read_b128 v[78:81], v213 offset:8896
	s_waitcnt lgkmcnt(0)
	v_mfma_f32_16x16x32_bf16 v[74:77], v[78:81], v[70:73], v[74:77]
	ds_read_b128 v[78:81], v213 offset:13056
	s_waitcnt lgkmcnt(0)
	v_mfma_f32_16x16x32_bf16 v[78:81], v[78:81], v[50:53], 0
	v_mfma_f32_16x16x32_bf16 v[78:81], v[82:85], v[54:57], v[78:81]
	ds_read_b128 v[82:85], v213 offset:13184
	s_waitcnt lgkmcnt(0)
	v_mfma_f32_16x16x32_bf16 v[78:81], v[82:85], v[58:61], v[78:81]
	ds_read_b128 v[82:85], v213 offset:13248
	ds_read_b128 v[86:89], v213 offset:17472
	s_waitcnt lgkmcnt(1)
	v_mfma_f32_16x16x32_bf16 v[78:81], v[82:85], v[70:73], v[78:81]
	ds_read_b128 v[82:85], v213 offset:17408
	ds_read_b128 v[90:93], v213 offset:21824
	ds_read_b128 v[94:97], v213 offset:26176
	s_waitcnt lgkmcnt(2)
	v_mfma_f32_16x16x32_bf16 v[82:85], v[82:85], v[50:53], 0
	ds_read_b128 v[98:101], v213 offset:30528
	v_mfma_f32_16x16x32_bf16 v[82:85], v[86:89], v[54:57], v[82:85]
	ds_read_b128 v[86:89], v213 offset:17536
	s_waitcnt lgkmcnt(0)
	v_mfma_f32_16x16x32_bf16 v[82:85], v[86:89], v[58:61], v[82:85]
	ds_read_b128 v[86:89], v213 offset:17600
	s_waitcnt lgkmcnt(0)
	v_mfma_f32_16x16x32_bf16 v[82:85], v[86:89], v[70:73], v[82:85]
	ds_read_b128 v[86:89], v213 offset:21760
	s_waitcnt lgkmcnt(0)
	v_mfma_f32_16x16x32_bf16 v[86:89], v[86:89], v[50:53], 0
	v_mfma_f32_16x16x32_bf16 v[86:89], v[90:93], v[54:57], v[86:89]
	ds_read_b128 v[90:93], v213 offset:21888
	s_waitcnt lgkmcnt(0)
	v_mfma_f32_16x16x32_bf16 v[86:89], v[90:93], v[58:61], v[86:89]
	ds_read_b128 v[90:93], v213 offset:21952
	s_waitcnt lgkmcnt(0)
	v_mfma_f32_16x16x32_bf16 v[86:89], v[90:93], v[70:73], v[86:89]
	ds_read_b128 v[90:93], v213 offset:26112
	s_waitcnt lgkmcnt(0)
	v_mfma_f32_16x16x32_bf16 v[90:93], v[90:93], v[50:53], 0
	v_mfma_f32_16x16x32_bf16 v[90:93], v[94:97], v[54:57], v[90:93]
	ds_read_b128 v[94:97], v213 offset:26240
	s_waitcnt lgkmcnt(0)
	v_mfma_f32_16x16x32_bf16 v[90:93], v[94:97], v[58:61], v[90:93]
	ds_read_b128 v[94:97], v213 offset:26304
	s_waitcnt lgkmcnt(0)
	v_mfma_f32_16x16x32_bf16 v[90:93], v[94:97], v[70:73], v[90:93]
	ds_read_b128 v[94:97], v213 offset:30464
	s_waitcnt lgkmcnt(0)
	v_mfma_f32_16x16x32_bf16 v[94:97], v[94:97], v[50:53], 0
	v_mfma_f32_16x16x32_bf16 v[94:97], v[98:101], v[54:57], v[94:97]
	ds_read_b128 v[98:101], v213 offset:30592
	s_waitcnt lgkmcnt(0)
	v_mfma_f32_16x16x32_bf16 v[94:97], v[98:101], v[58:61], v[94:97]
	ds_read_b128 v[98:101], v213 offset:30656
	ds_read_b128 v[102:105], v213 offset:34880
	s_waitcnt lgkmcnt(1)
	v_mfma_f32_16x16x32_bf16 v[94:97], v[98:101], v[70:73], v[94:97]
	ds_read_b128 v[98:101], v213 offset:34816
	ds_read_b128 v[106:109], v213 offset:39232
	ds_read_b128 v[110:113], v213 offset:43584
	s_waitcnt lgkmcnt(2)
	v_mfma_f32_16x16x32_bf16 v[98:101], v[98:101], v[50:53], 0
	ds_read_b128 v[114:117], v213 offset:47936
	v_mfma_f32_16x16x32_bf16 v[98:101], v[102:105], v[54:57], v[98:101]
	ds_read_b128 v[102:105], v213 offset:34944
	s_waitcnt lgkmcnt(0)
	v_mfma_f32_16x16x32_bf16 v[98:101], v[102:105], v[58:61], v[98:101]
	ds_read_b128 v[102:105], v213 offset:35008
	s_waitcnt lgkmcnt(0)
	v_mfma_f32_16x16x32_bf16 v[98:101], v[102:105], v[70:73], v[98:101]
	ds_read_b128 v[102:105], v213 offset:39168
	s_waitcnt lgkmcnt(0)
	v_mfma_f32_16x16x32_bf16 v[102:105], v[102:105], v[50:53], 0
	v_mfma_f32_16x16x32_bf16 v[102:105], v[106:109], v[54:57], v[102:105]
	ds_read_b128 v[106:109], v213 offset:39296
	s_waitcnt lgkmcnt(0)
	v_mfma_f32_16x16x32_bf16 v[102:105], v[106:109], v[58:61], v[102:105]
	ds_read_b128 v[106:109], v213 offset:39360
	s_waitcnt lgkmcnt(0)
	v_mfma_f32_16x16x32_bf16 v[102:105], v[106:109], v[70:73], v[102:105]
	ds_read_b128 v[106:109], v213 offset:43520
	s_waitcnt lgkmcnt(0)
	v_mfma_f32_16x16x32_bf16 v[106:109], v[106:109], v[50:53], 0
	v_mfma_f32_16x16x32_bf16 v[106:109], v[110:113], v[54:57], v[106:109]
	ds_read_b128 v[110:113], v213 offset:43648
	s_waitcnt lgkmcnt(0)
	v_mfma_f32_16x16x32_bf16 v[106:109], v[110:113], v[58:61], v[106:109]
	ds_read_b128 v[110:113], v213 offset:43712
	s_waitcnt lgkmcnt(0)
	v_mfma_f32_16x16x32_bf16 v[106:109], v[110:113], v[70:73], v[106:109]
	ds_read_b128 v[110:113], v213 offset:47872
	s_waitcnt lgkmcnt(0)
	v_mfma_f32_16x16x32_bf16 v[110:113], v[110:113], v[50:53], 0
	v_mfma_f32_16x16x32_bf16 v[110:113], v[114:117], v[54:57], v[110:113]
	ds_read_b128 v[114:117], v213 offset:48000
	s_waitcnt lgkmcnt(0)
	v_mfma_f32_16x16x32_bf16 v[110:113], v[114:117], v[58:61], v[110:113]
	ds_read_b128 v[114:117], v213 offset:48064
	ds_read_b128 v[118:121], v213 offset:52288
	s_waitcnt lgkmcnt(1)
	v_mfma_f32_16x16x32_bf16 v[110:113], v[114:117], v[70:73], v[110:113]
	ds_read_b128 v[114:117], v213 offset:52224
	ds_read_b128 v[122:125], v213 offset:56640
	ds_read_b128 v[126:129], v213 offset:60992
	s_waitcnt lgkmcnt(2)
	v_mfma_f32_16x16x32_bf16 v[114:117], v[114:117], v[50:53], 0
	ds_read_b128 v[132:135], v213 offset:65344
	v_mfma_f32_16x16x32_bf16 v[114:117], v[118:121], v[54:57], v[114:117]
	ds_read_b128 v[118:121], v213 offset:52352
	s_waitcnt lgkmcnt(0)
	v_mfma_f32_16x16x32_bf16 v[114:117], v[118:121], v[58:61], v[114:117]
	ds_read_b128 v[118:121], v213 offset:52416
	s_waitcnt lgkmcnt(0)
	v_mfma_f32_16x16x32_bf16 v[114:117], v[118:121], v[70:73], v[114:117]
	ds_read_b128 v[118:121], v213 offset:56576
	s_waitcnt lgkmcnt(0)
	v_mfma_f32_16x16x32_bf16 v[118:121], v[118:121], v[50:53], 0
	v_mfma_f32_16x16x32_bf16 v[118:121], v[122:125], v[54:57], v[118:121]
	ds_read_b128 v[122:125], v213 offset:56704
	s_waitcnt lgkmcnt(0)
	v_mfma_f32_16x16x32_bf16 v[118:121], v[122:125], v[58:61], v[118:121]
	ds_read_b128 v[122:125], v213 offset:56768
	s_waitcnt lgkmcnt(0)
	v_mfma_f32_16x16x32_bf16 v[118:121], v[122:125], v[70:73], v[118:121]
	ds_read_b128 v[122:125], v213 offset:60928
	s_waitcnt lgkmcnt(0)
	v_mfma_f32_16x16x32_bf16 v[122:125], v[122:125], v[50:53], 0
	v_mfma_f32_16x16x32_bf16 v[122:125], v[126:129], v[54:57], v[122:125]
	ds_read_b128 v[126:129], v213 offset:61056
	s_waitcnt lgkmcnt(0)
	v_mfma_f32_16x16x32_bf16 v[122:125], v[126:129], v[58:61], v[122:125]
	ds_read_b128 v[126:129], v213 offset:61120
	s_waitcnt lgkmcnt(0)
	v_mfma_f32_16x16x32_bf16 v[122:125], v[126:129], v[70:73], v[122:125]
	ds_read_b128 v[126:129], v213 offset:65280
	s_waitcnt lgkmcnt(0)
	v_mfma_f32_16x16x32_bf16 v[126:129], v[126:129], v[50:53], 0
	v_mfma_f32_16x16x32_bf16 v[126:129], v[132:135], v[54:57], v[126:129]
	ds_read_b128 v[132:135], v213 offset:65408
	s_waitcnt lgkmcnt(0)
	v_mfma_f32_16x16x32_bf16 v[126:129], v[132:135], v[58:61], v[126:129]
	ds_read_b128 v[132:135], v213 offset:65472
	s_waitcnt lgkmcnt(0)
	v_mfma_f32_16x16x32_bf16 v[126:129], v[132:135], v[70:73], v[126:129]
	v_mad_u64_u32 v[132:133], s[70:71], v131, s3, v[138:139]
	v_mad_i32_i24 v133, s31, v216, v133
	global_load_dwordx4 v[142:145], v[132:133], off
	global_load_dwordx4 v[146:149], v[132:133], off offset:64
	global_load_dwordx4 v[150:153], v[132:133], off offset:128
	global_load_dwordx4 v[154:157], v[132:133], off offset:192
	v_cndmask_b32_e64 v131, 0, 1, s[94:95]
	v_cmp_ne_u32_e64 s[74:75], 1, v131
	s_mulk_i32 s31, 0x600
	s_cbranch_vccz .LBB0_665
	v_cndmask_b32_e64 v131, 0, 1, s[86:87]
	v_cmp_ne_u32_e64 s[70:71], 1, v131
	s_andn2_b64 vcc, exec, s[86:87]
	s_cbranch_vccz .LBB0_666
